# v12 plus three small exact changes: down/combine phases reuse the LDS block tables, memory-attention query gathers issued before the K/V staging loop, LN_in variance wave sum by DPP butterfly
# speedup vs baseline: 1.0006x; 1.0006x over previous
; #define IN(k) ((const float*)gptr(ldp(PT, k)))
; __device__ __forceinline__ void ln_rows_pre(f32x4 (&v)[4], const LnAff& a) {
;     float s = 0.f;
; #pragma unroll
;     for (int j = 0; j < 4; ++j) s += (v[j][0] + v[j][1]) + (v[j][2] + v[j][3]);
;     const float mean = wave_sum(s) * (1.f / D); float s2 = 0.f;
; #pragma unroll
;     for (int j = 0; j < 4; ++j) { v[j] = v[j] - mean; s2 += (v[j][0] * v[j][0] + v[j][1] * v[j][1]) + (v[j][2] * v[j][2] + v[j][3] * v[j][3]); }
;     const float rstd = 1.f / sqrtf(wave_sum(s2) * (1.f / D) + LN_EPS);
; __global__ void __launch_bounds__(NWAVES * 64, 2) fwd(Args args) {
;     ...
;         for (int m = F.gw; m < M; m += F.NGW) { const float* xp = IN(0) + (size_t)m * D; f32x4 v[4];
; #pragma unroll
;             for (int j = 0; j < 4; ++j) v[j] = *(const f32x4*)(xp + 4 * lane + 256 * j);
.LBB0_250:
	ds_read_b64 v[38:39], v44
	v_lshl_add_u64 v[40:41], s[58:59], 0, v[34:35]
	v_add_co_u32_e32 v42, vcc, s13, v40
	v_lshl_add_u64 v[48:49], s[58:59], 0, v[32:33]
	s_nop 0
	v_addc_co_u32_e32 v43, vcc, 0, v41, vcc
	s_waitcnt lgkmcnt(0)
	v_readfirstlane_b32 s1, v39
	v_readfirstlane_b32 s0, v38
	v_add_co_u32_e32 v40, vcc, s16, v48
	s_nop 0
	v_lshl_add_u64 v[38:39], s[0:1], 0, v[36:37]
	v_addc_co_u32_e32 v41, vcc, 0, v49, vcc
	global_load_dwordx4 v[48:51], v[38:39], off
	global_load_dwordx4 v[52:55], v[38:39], off offset:1024
	global_load_dwordx4 v[56:59], v[38:39], off offset:2048
	global_load_dwordx4 v[60:63], v[38:39], off offset:3072
	v_mov_b32_e32 v65, v80
	v_mov_b32_e32 v66, v80
	s_add_i32 s6, s6, s8
	v_lshlrev_b32_e32 v38, 2, v65
	v_lshlrev_b32_e32 v39, 2, v66
	v_xor_b32_e32 v65, 4, v38
	v_xor_b32_e32 v78, 8, v38
	v_xor_b32_e32 v79, 16, v38
	v_xor_b32_e32 v81, 32, v38
	v_xor_b32_e32 v82, 64, v38
	v_xor_b32_e32 v83, 0x80, v38
	v_xor_b32_e32 v84, 4, v39
	v_xor_b32_e32 v85, 8, v39
	v_xor_b32_e32 v86, 16, v39
	v_xor_b32_e32 v87, 32, v39
	v_xor_b32_e32 v88, 64, v39
	v_xor_b32_e32 v89, 0x80, v39
	v_lshl_add_u64 v[32:33], v[32:33], 0, s[2:3]
	v_lshl_add_u64 v[34:35], v[34:35], 0, s[4:5]
	s_cmpk_gt_i32 s6, 0x3fff
	v_lshl_add_u64 v[36:37], v[36:37], 0, s[10:11]
	s_waitcnt vmcnt(3)
	v_mov_b32_e32 v38, v49
	v_mov_b32_e32 v39, v50
	v_mov_b32_e32 v66, v48
	v_mov_b32_e32 v67, v51
	s_waitcnt vmcnt(2)
	v_mov_b32_e32 v68, v53
	v_mov_b32_e32 v69, v54
	v_mov_b32_e32 v70, v52
	v_mov_b32_e32 v71, v55
	v_pk_add_f32 v[38:39], v[38:39], v[66:67]
	v_pk_add_f32 v[66:67], v[68:69], v[70:71]
	v_add_f32_e32 v70, v38, v39
	v_pk_add_f32 v[38:39], v[66:67], v[66:67] op_sel:[0,1] op_sel_hi:[1,0]
	s_waitcnt vmcnt(1)
	v_add_f32_e32 v72, v56, v57
	v_add_f32_e32 v74, v58, v59
	s_waitcnt vmcnt(0)
	v_mov_b32_e32 v77, v60
	v_mov_b32_e32 v73, v62
	v_mov_b32_e32 v75, v63
	v_add_f32_e32 v76, 0, v70
	v_mov_b32_e32 v39, v61
	v_pk_add_f32 v[68:69], v[72:73], v[74:75]
	v_pk_add_f32 v[38:39], v[76:77], v[38:39]
	s_nop 0
	v_pk_add_f32 v[38:39], v[38:39], v[68:69]
	s_nop 0
	v_add_f32_e32 v38, v38, v39
	s_nop 1
	v_add_f32_dpp v38, v38, v38 quad_perm:[1,0,3,2] row_mask:0xf bank_mask:0xf
	s_nop 1
	v_add_f32_dpp v38, v38, v38 quad_perm:[2,3,0,1] row_mask:0xf bank_mask:0xf
	s_nop 1
	v_add_f32_dpp v38, v38, v38 row_half_mirror row_mask:0xf bank_mask:0xf
	s_nop 1
	v_add_f32_dpp v38, v38, v38 row_mirror row_mask:0xf bank_mask:0xf
	v_mov_b32_e32 v39, v38
	v_mov_b32_e32 v83, v38
	s_nop 1
	v_permlane16_swap_b32 v39, v83
	v_add_f32_e32 v38, v39, v83
	v_mov_b32_e32 v39, v38
	v_mov_b32_e32 v83, v38
	s_nop 1
	v_permlane32_swap_b32 v39, v83
	v_add_f32_e32 v65, v39, v83
	v_fmamk_f32 v39, v65, 0xba800000, v49
	v_fmamk_f32 v38, v65, 0xba800000, v48
	v_fmamk_f32 v51, v65, 0xba800000, v51
	v_fmac_f32_e32 v50, 0xba800000, v65
	v_fmamk_f32 v49, v65, 0xba800000, v53
	v_fmamk_f32 v48, v65, 0xba800000, v52
	v_fmamk_f32 v55, v65, 0xba800000, v55
	v_fmac_f32_e32 v54, 0xba800000, v65
	v_fmamk_f32 v53, v65, 0xba800000, v57
	v_fmamk_f32 v52, v65, 0xba800000, v56
	v_fmamk_f32 v57, v65, 0xba800000, v63
	v_fmamk_f32 v56, v65, 0xba800000, v62
	v_pk_mul_f32 v[62:63], v[50:51], v[50:51]
	v_pk_mul_f32 v[66:67], v[38:39], v[38:39]
	v_pk_mul_f32 v[68:69], v[54:55], v[54:55]
	v_pk_mul_f32 v[70:71], v[48:49], v[48:49]
	v_fmac_f32_e32 v58, 0xba800000, v65
	v_pk_mov_b32 v[76:77], v[66:67], v[62:63] op_sel:[1,0]
	v_mov_b32_e32 v67, v63
	v_pk_mov_b32 v[62:63], v[70:71], v[68:69] op_sel:[1,0]
	v_mov_b32_e32 v71, v69
	v_fmamk_f32 v59, v65, 0xba800000, v59
	v_mul_f32_e32 v72, v52, v52
	v_mul_f32_e32 v74, v58, v58
	v_pk_add_f32 v[66:67], v[76:77], v[66:67]
	v_pk_add_f32 v[62:63], v[62:63], v[70:71]
	v_fmamk_f32 v61, v65, 0xba800000, v61
	v_fmac_f32_e32 v60, 0xba800000, v65
	v_pk_fma_f32 v[68:69], v[52:53], v[52:53], v[72:73] op_sel_hi:[1,1,0]
	v_pk_fma_f32 v[72:73], v[58:59], v[58:59], v[74:75] op_sel_hi:[1,1,0]
	v_pk_add_f32 v[66:67], v[66:67], v[66:67] op_sel_hi:[0,1]
	v_pk_add_f32 v[62:63], v[62:63], v[62:63] op_sel_hi:[0,1]
	v_mul_f32_e32 v68, v60, v60
	v_mul_f32_e32 v72, v61, v61
	v_mul_f32_e32 v66, v56, v56
	v_mul_f32_e32 v62, v57, v57
	v_pk_add_f32 v[68:69], v[68:69], v[72:73]
	v_pk_add_f32 v[62:63], v[66:67], v[62:63]
	s_nop 0
	v_pk_add_f32 v[62:63], v[68:69], v[62:63]
	s_nop 0
	v_add_f32_e32 v62, v62, v63
	s_nop 1
	v_add_f32_dpp v62, v62, v62 quad_perm:[1,0,3,2] row_mask:0xf bank_mask:0xf
	s_nop 1
	v_add_f32_dpp v62, v62, v62 quad_perm:[2,3,0,1] row_mask:0xf bank_mask:0xf
	s_nop 1
	v_add_f32_dpp v62, v62, v62 row_half_mirror row_mask:0xf bank_mask:0xf
	s_nop 1
	v_add_f32_dpp v62, v62, v62 row_mirror row_mask:0xf bank_mask:0xf
	v_mov_b32_e32 v63, v62
	v_mov_b32_e32 v65, v62
	s_nop 1
	v_permlane16_swap_b32 v63, v65
	v_add_f32_e32 v62, v63, v65
	v_mov_b32_e32 v63, v62
	v_mov_b32_e32 v65, v62
	s_nop 1
	v_permlane32_swap_b32 v63, v65
	v_add_f32_e32 v62, v63, v65
	v_fmamk_f32 v62, v62, 0x3a800000, v45
	v_mul_f32_e32 v63, 0x4f800000, v62
	v_cmp_gt_f32_e32 vcc, s7, v62
	s_nop 1
	v_cndmask_b32_e32 v62, v62, v63, vcc
	v_sqrt_f32_e32 v63, v62
	s_nop 0
	v_add_u32_e32 v65, -1, v63
	v_add_u32_e32 v66, 1, v63
	v_fma_f32 v67, -v65, v63, v62
	v_fma_f32 v68, -v66, v63, v62
	v_cmp_ge_f32_e64 s[0:1], 0, v67
	s_nop 1
	v_cndmask_b32_e64 v63, v63, v65, s[0:1]
	v_cmp_lt_f32_e64 s[0:1], 0, v68
	s_nop 1
	v_cndmask_b32_e64 v63, v63, v66, s[0:1]
	v_mul_f32_e32 v65, 0x37800000, v63
	v_cndmask_b32_e32 v63, v63, v65, vcc
	v_cmp_class_f32_e32 vcc, v62, v46
	s_nop 1
	v_cndmask_b32_e32 v62, v63, v62, vcc
	v_div_scale_f32 v63, s[0:1], v62, v62, 1.0
	v_rcp_f32_e32 v66, v63
	v_div_scale_f32 v65, vcc, 1.0, v62, 1.0
	v_fma_f32 v67, -v63, v66, 1.0
; __device__ __forceinline__ unsigned pk2(float lo, float hi) { return f2bf(lo) | (f2bf(hi) << 16); }
; __device__ __forceinline__ unsigned q8_(float x, float s) { return (unsigned)(int)__builtin_rintf(fminf(fmaxf(x * s, -127.f), 127.f)) & 255u; }
; __device__ __forceinline__ unsigned q8x4(float a, float b, float c, float d, float s) { return q8_(a, s) | (q8_(b, s) << 8) | (q8_(c, s) << 16) | (q8_(d, s) << 24); }
; __device__ __forceinline__ void ln_rows_pre(f32x4 (&v)[4], const LnAff& a) {
;     ...
;     for (int j = 0; j < 4; ++j) v[j] = v[j] * rstd * a.g[j] + a.b[j];
; }
; __device__ __forceinline__ void store_row_f32_bf16(const f32x4 (&v)[4], float* of, bf16* ob, int lane) {
; #pragma unroll
;     for (int j = 0; j < 4; ++j) { if (of) *(f32x4*)(of + 4 * lane + 256 * j) = v[j];
;         if (ob) { v2u w; w.x = pk2(v[j][0], v[j][1]); w.y = pk2(v[j][2], v[j][3]); *(v2u*)(ob + 4 * lane + 256 * j) = w; } }
; __device__ __forceinline__ void store_row_fp8(const f32x4 (&v)[4], unsigned char* o8, int lane) {
; #pragma unroll
;     for (int j = 0; j < 4; ++j) *(unsigned*)(o8 + 4 * lane + 256 * j) = q8x4(v[j][0], v[j][1], v[j][2], v[j][3], QS_H);
	v_fmac_f32_e32 v66, v67, v66
	v_mul_f32_e32 v67, v65, v66
	v_fma_f32 v68, -v63, v67, v65
	v_fmac_f32_e32 v67, v68, v66
	v_fma_f32 v63, -v63, v67, v65
	v_div_fmas_f32 v63, v63, v66, v67
	v_div_fixup_f32 v62, v63, v62, 1.0
	v_pk_mul_f32 v[38:39], v[38:39], v[62:63] op_sel_hi:[1,0]
	v_pk_mul_f32 v[48:49], v[48:49], v[62:63] op_sel_hi:[1,0]
	v_pk_mul_f32 v[54:55], v[54:55], v[62:63] op_sel_hi:[1,0]
	v_pk_mul_f32 v[50:51], v[50:51], v[62:63] op_sel_hi:[1,0]
	v_pk_mul_f32 v[52:53], v[52:53], v[62:63] op_sel_hi:[1,0]
	v_pk_mul_f32 v[58:59], v[58:59], v[62:63] op_sel_hi:[1,0]
	v_pk_mul_f32 v[60:61], v[60:61], v[62:63] op_sel_hi:[1,0]
	v_pk_mul_f32 v[56:57], v[56:57], v[62:63] op_sel_hi:[1,0]
	v_pk_fma_f32 v[38:39], v[0:1], v[38:39], v[8:9]
	v_pk_fma_f32 v[54:55], v[6:7], v[54:55], v[14:15]
	v_pk_fma_f32 v[48:49], v[4:5], v[48:49], v[12:13]
	v_pk_fma_f32 v[50:51], v[2:3], v[50:51], v[10:11]
	v_pk_fma_f32 v[58:59], v[18:19], v[58:59], v[26:27]
	v_pk_fma_f32 v[52:53], v[16:17], v[52:53], v[24:25]
	v_pk_fma_f32 v[56:57], v[22:23], v[56:57], v[30:31]
	v_pk_fma_f32 v[60:61], v[20:21], v[60:61], v[28:29]
	v_bfe_u32 v63, v39, 16, 1
	v_bfe_u32 v67, v48, 16, 1
	v_bfe_u32 v69, v54, 16, 1
	v_mul_f32_e32 v81, 0x41cb3333, v39
	v_bfe_u32 v62, v38, 16, 1
	v_bfe_u32 v65, v50, 16, 1
	v_bfe_u32 v66, v51, 16, 1
	v_bfe_u32 v68, v49, 16, 1
	v_bfe_u32 v70, v55, 16, 1
	v_bfe_u32 v71, v52, 16, 1
	v_bfe_u32 v72, v53, 16, 1
	v_bfe_u32 v73, v58, 16, 1
	v_bfe_u32 v76, v61, 16, 1
	v_bfe_u32 v77, v56, 16, 1
	v_mul_f32_e32 v79, 0x41cb3333, v38
	v_mul_f32_e32 v82, 0x41cb3333, v50
	v_mul_f32_e32 v83, 0x41cb3333, v51
	v_mul_f32_e32 v84, 0x41cb3333, v48
	v_mul_f32_e32 v85, 0x41cb3333, v49
	v_mul_f32_e32 v86, 0x41cb3333, v54
	v_mul_f32_e32 v89, 0x41cb3333, v53
	v_mul_f32_e32 v93, 0x41cb3333, v61
	v_add3_u32 v39, v39, v63, s9
	v_add3_u32 v48, v48, v67, s9
	v_add3_u32 v54, v54, v69, s9
	v_med3_f32 v63, v81, s14, v47
	v_bfe_u32 v74, v59, 16, 1
	v_bfe_u32 v75, v60, 16, 1
	v_bfe_u32 v78, v57, 16, 1
	v_mul_f32_e32 v87, 0x41cb3333, v55
	v_mul_f32_e32 v88, 0x41cb3333, v52
	v_mul_f32_e32 v90, 0x41cb3333, v58
	v_mul_f32_e32 v91, 0x41cb3333, v59
	v_mul_f32_e32 v92, 0x41cb3333, v60
	v_mul_f32_e32 v94, 0x41cb3333, v56
	v_mul_f32_e32 v95, 0x41cb3333, v57
	v_add3_u32 v38, v38, v62, s9
	v_add3_u32 v50, v50, v65, s9
	v_add3_u32 v51, v51, v66, s9
	v_add3_u32 v49, v49, v68, s9
	v_add3_u32 v55, v55, v70, s9
	v_add3_u32 v52, v52, v71, s9
	v_add3_u32 v53, v53, v72, s9
	v_add3_u32 v58, v58, v73, s9
	v_add3_u32 v61, v61, v76, s9
	v_add3_u32 v56, v56, v77, s9
	v_med3_f32 v62, v79, s14, v47
	v_med3_f32 v65, v82, s14, v47
	v_med3_f32 v66, v83, s14, v47
	v_med3_f32 v68, v85, s14, v47
	v_med3_f32 v72, v89, s14, v47
	v_med3_f32 v76, v93, s14, v47
	v_lshrrev_b32_e32 v48, 16, v48
	v_lshrrev_b32_e32 v54, 16, v54
	v_rndne_f32_e32 v63, v63
	v_add3_u32 v59, v59, v74, s9
	v_add3_u32 v60, v60, v75, s9
	v_add3_u32 v57, v57, v78, s9
	v_med3_f32 v67, v84, s14, v47
	v_med3_f32 v69, v86, s14, v47
	v_med3_f32 v70, v87, s14, v47
	v_med3_f32 v71, v88, s14, v47
	v_med3_f32 v73, v90, s14, v47
	v_med3_f32 v74, v91, s14, v47
	v_med3_f32 v75, v92, s14, v47
	v_med3_f32 v77, v94, s14, v47
	v_med3_f32 v78, v95, s14, v47
	v_lshrrev_b32_e32 v38, 16, v38
	v_lshrrev_b32_e32 v50, 16, v50
	v_lshrrev_b32_e32 v52, 16, v52
	v_lshrrev_b32_e32 v58, 16, v58
	v_lshrrev_b32_e32 v56, 16, v56
	v_rndne_f32_e32 v62, v62
	v_rndne_f32_e32 v65, v65
	v_rndne_f32_e32 v66, v66
	v_rndne_f32_e32 v68, v68
	v_rndne_f32_e32 v72, v72
	v_rndne_f32_e32 v76, v76
	v_and_or_b32 v48, v49, s12, v48
	v_and_or_b32 v49, v55, s12, v54
	v_cvt_i32_f32_e32 v55, v63
	v_lshrrev_b32_e32 v60, 16, v60
	v_rndne_f32_e32 v67, v67
	v_rndne_f32_e32 v69, v69
	v_rndne_f32_e32 v70, v70
	v_rndne_f32_e32 v71, v71
	v_rndne_f32_e32 v73, v73
	v_rndne_f32_e32 v74, v74
	v_rndne_f32_e32 v75, v75
	v_rndne_f32_e32 v77, v77
	v_rndne_f32_e32 v78, v78
	v_and_or_b32 v38, v39, s12, v38
	v_and_or_b32 v39, v51, s12, v50
	v_and_or_b32 v50, v53, s12, v52
	v_and_or_b32 v51, v59, s12, v58
	v_and_or_b32 v53, v57, s12, v56
	v_cvt_i32_f32_e32 v54, v62
	v_cvt_i32_f32_sdwa v56, v65 dst_sel:WORD_1 dst_unused:UNUSED_PAD src0_sel:DWORD
	v_cvt_i32_f32_e32 v57, v66
	v_cvt_i32_f32_e32 v59, v68
	v_cvt_i32_f32_e32 v63, v72
	v_cvt_i32_f32_e32 v68, v76
	v_and_or_b32 v52, v61, s12, v60
	v_cvt_i32_f32_e32 v58, v67
	v_cvt_i32_f32_sdwa v60, v69 dst_sel:WORD_1 dst_unused:UNUSED_PAD src0_sel:DWORD
	v_cvt_i32_f32_e32 v61, v70
	v_cvt_i32_f32_e32 v62, v71
	v_cvt_i32_f32_sdwa v65, v73 dst_sel:WORD_1 dst_unused:UNUSED_PAD src0_sel:DWORD
	v_cvt_i32_f32_e32 v66, v74
	v_cvt_i32_f32_e32 v67, v75
	v_cvt_i32_f32_sdwa v69, v77 dst_sel:WORD_1 dst_unused:UNUSED_PAD src0_sel:DWORD
	v_cvt_i32_f32_e32 v70, v78
	global_store_dwordx2 v[42:43], v[38:39], off
	global_store_dwordx2 v[42:43], v[48:49], off offset:512
	global_store_dwordx2 v[42:43], v[50:51], off offset:1024
	global_store_dwordx2 v[42:43], v[52:53], off offset:1536
	v_lshlrev_b32_e32 v38, 8, v55
	v_and_b32_e32 v39, 0xff0000, v56
	v_perm_b32 v42, v57, v54, s15
	v_lshlrev_b32_e32 v43, 8, v59
	v_lshlrev_b32_e32 v50, 8, v63
	v_lshlrev_b32_e32 v53, 8, v68
	v_and_b32_e32 v38, 0xff00, v38
	v_and_b32_e32 v48, 0xff0000, v60
	v_perm_b32 v49, v61, v58, s15
	v_and_b32_e32 v51, 0xff0000, v65
	v_perm_b32 v52, v66, v62, s15
	v_and_b32_e32 v54, 0xff0000, v69
	v_perm_b32 v55, v70, v67, s15
	v_and_b32_e32 v43, 0xff00, v43
	v_and_b32_e32 v50, 0xff00, v50
	v_and_b32_e32 v53, 0xff00, v53
	v_or3_b32 v38, v42, v38, v39
	v_or3_b32 v39, v49, v43, v48
	v_or3_b32 v42, v52, v50, v51
	v_or3_b32 v43, v55, v53, v54
	global_store_dword v[40:41], v38, off
	global_store_dword v[40:41], v39, off offset:256
	global_store_dword v[40:41], v42, off offset:512
	global_store_dword v[40:41], v43, off offset:768
	s_cbranch_scc0 .LBB0_250
